# grid-barrier poll loops: s_sleep 1 removed (tighter polling) on top of v61
# baseline (speedup 1.0000x reference)
.LBB0_87:
	global_load_dword v16, v17, s[60:61] offset:1024 sc1
	global_load_dword v0, v17, s[60:61] offset:1280 sc1
	global_load_dword v2, v17, s[60:61] offset:1536 sc1
	global_load_dword v3, v17, s[60:61] offset:1792 sc1
	global_load_dword v4, v17, s[60:61] offset:2048 sc1
	global_load_dword v5, v17, s[60:61] offset:2304 sc1
	global_load_dword v6, v17, s[60:61] offset:2560 sc1
	global_load_dword v7, v17, s[60:61] offset:2816 sc1
	global_load_dword v8, v17, s[60:61] offset:3072 sc1
	global_load_dword v9, v17, s[60:61] offset:3328 sc1
	global_load_dword v10, v17, s[60:61] offset:3584 sc1
	global_load_dword v11, v17, s[60:61] offset:3840 sc1
	global_load_dword v12, v17, s[4:5] sc1
	global_load_dword v13, v17, s[6:7] sc1
	global_load_dword v14, v17, s[8:9] sc1
	global_load_dword v15, v17, s[10:11] sc1
	s_mov_b64 s[12:13], -1
	s_mov_b64 s[14:15], -1
	s_waitcnt vmcnt(14)
	v_add_u32_e32 v18, v0, v16
	s_waitcnt vmcnt(13)
	v_add_u32_e32 v18, v18, v2
	s_waitcnt vmcnt(12)
	v_add_u32_e32 v18, v18, v3
	s_waitcnt vmcnt(11)
	v_add_u32_e32 v18, v18, v4
	s_waitcnt vmcnt(10)
	v_add_u32_e32 v18, v18, v5
	s_waitcnt vmcnt(9)
	v_add_u32_e32 v18, v18, v6
	s_waitcnt vmcnt(8)
	v_add_u32_e32 v18, v18, v7
	s_waitcnt vmcnt(7)
	v_add_u32_e32 v18, v18, v8
	s_waitcnt vmcnt(6)
	v_add_u32_e32 v18, v18, v9
	s_waitcnt vmcnt(5)
	v_add_u32_e32 v18, v18, v10
	s_waitcnt vmcnt(4)
	v_add_u32_e32 v18, v18, v11
	s_waitcnt vmcnt(3)
	v_add_u32_e32 v18, v18, v12
	s_waitcnt vmcnt(2)
	v_add_u32_e32 v18, v18, v13
	s_waitcnt vmcnt(1)
	v_add_u32_e32 v18, v18, v14
	s_waitcnt vmcnt(0)
	v_add_u32_e32 v18, v18, v15
	v_cmp_eq_u32_e32 vcc, s19, v18
	s_cbranch_vccnz .LBB0_86
	s_and_b32 s12, s20, 0xff
	s_cmp_eq_u32 s12, 0
	s_mov_b64 s[12:13], -1
	s_mov_b64 s[16:17], -1
	s_cbranch_scc1 .LBB0_91
	s_and_b64 vcc, exec, s[16:17]
	s_cbranch_vccz .LBB0_86

.LBB0_105:
	s_and_b32 s16, s20, 0xff
	s_mov_b64 s[14:15], -1
	s_cmp_lg_u32 s16, 0
	s_mov_b64 s[18:19], -1
	s_cbranch_scc0 .LBB0_108
	s_and_b64 vcc, exec, s[18:19]
	s_cbranch_vccz .LBB0_104

.LBB0_122:
	s_and_b32 s16, s22, 0xff
	s_cmp_lg_u32 s16, 0
	s_mov_b64 s[18:19], -1
	s_cbranch_scc0 .LBB0_125
	s_mov_b64 s[20:21], -1
	s_and_b64 vcc, exec, s[18:19]
	s_cbranch_vccz .LBB0_121

.LBB0_457:
	v_readlane_b32 s2, v250, 25
	v_readlane_b32 s3, v250, 26
	global_load_dword v12, v173, s[60:61] offset:1024 sc1
	global_load_dword v0, v173, s[60:61] offset:1280 sc1
	global_load_dword v2, v173, s[60:61] offset:1536 sc1
	global_load_dword v3, v173, s[60:61] offset:1792 sc1
	global_load_dword v4, v173, s[60:61] offset:2048 sc1
	global_load_dword v5, v173, s[60:61] offset:2304 sc1
	global_load_dword v6, v173, s[60:61] offset:2560 sc1
	global_load_dword v7, v173, s[60:61] offset:2816 sc1
	global_load_dword v8, v173, s[60:61] offset:3072 sc1
	global_load_dword v9, v173, s[60:61] offset:3328 sc1
	global_load_dword v10, v173, s[60:61] offset:3584 sc1
	global_load_dword v11, v173, s[60:61] offset:3840 sc1
	global_load_dword v13, v173, s[2:3] sc1
	v_readlane_b32 s2, v250, 27
	v_readlane_b32 s3, v250, 28
	s_mov_b64 s[8:9], -1
	s_mov_b64 s[10:11], -1
	s_waitcnt vmcnt(11)
	v_add_u32_e32 v17, v0, v12
	s_nop 0
	global_load_dword v14, v173, s[2:3] sc1
	v_readlane_b32 s2, v250, 29
	v_readlane_b32 s3, v250, 30
	s_waitcnt vmcnt(11)
	v_add_u32_e32 v17, v17, v2
	s_waitcnt vmcnt(10)
	v_add_u32_e32 v17, v17, v3
	s_waitcnt vmcnt(9)
	v_add_u32_e32 v17, v17, v4
	s_waitcnt vmcnt(8)
	v_add_u32_e32 v17, v17, v5
	s_waitcnt vmcnt(7)
	v_add_u32_e32 v17, v17, v6
	global_load_dword v15, v173, s[2:3] sc1
	v_readlane_b32 s2, v250, 31
	v_readlane_b32 s3, v250, 32
	s_waitcnt vmcnt(7)
	v_add_u32_e32 v17, v17, v7
	s_waitcnt vmcnt(6)
	v_add_u32_e32 v17, v17, v8
	s_waitcnt vmcnt(5)
	v_add_u32_e32 v17, v17, v9
	s_waitcnt vmcnt(4)
	v_add_u32_e32 v17, v17, v10
	s_waitcnt vmcnt(3)
	v_add_u32_e32 v17, v17, v11
	global_load_dword v16, v173, s[2:3] sc1
	s_waitcnt vmcnt(3)
	v_add_u32_e32 v17, v17, v13
	s_waitcnt vmcnt(2)
	v_add_u32_e32 v17, v17, v14
	s_waitcnt vmcnt(1)
	v_add_u32_e32 v17, v17, v15
	s_waitcnt vmcnt(0)
	v_add_u32_e32 v17, v17, v16
	v_cmp_eq_u32_e32 vcc, s12, v17
	s_cbranch_vccnz .LBB0_456
	s_and_b32 s2, s13, 0xff
	s_cmp_eq_u32 s2, 0
	s_mov_b64 s[2:3], -1
	s_cbranch_scc1 .LBB0_461
	s_and_b64 vcc, exec, s[2:3]
	s_cbranch_vccz .LBB0_456

.LBB0_475:
	s_and_b32 s2, s1, 0xff
	s_mov_b64 s[18:19], -1
	s_cmp_lg_u32 s2, 0
	s_mov_b64 s[2:3], -1
	s_cbranch_scc0 .LBB0_478
	s_and_b64 vcc, exec, s[2:3]
	s_cbranch_vccz .LBB0_474

.LBB0_492:
	s_and_b32 s2, s1, 0xff
	s_mov_b64 s[16:17], -1
	s_cmp_lg_u32 s2, 0
	s_mov_b64 s[2:3], -1
	s_cbranch_scc0 .LBB0_495
	s_and_b64 vcc, exec, s[2:3]
	s_cbranch_vccz .LBB0_491

.LBB0_589:
	v_readlane_b32 s2, v250, 25
	v_readlane_b32 s3, v250, 26
	global_load_dword v12, v173, s[60:61] offset:1024 sc1
	global_load_dword v0, v173, s[60:61] offset:1280 sc1
	global_load_dword v2, v173, s[60:61] offset:1536 sc1
	global_load_dword v3, v173, s[60:61] offset:1792 sc1
	global_load_dword v4, v173, s[60:61] offset:2048 sc1
	global_load_dword v5, v173, s[60:61] offset:2304 sc1
	global_load_dword v6, v173, s[60:61] offset:2560 sc1
	global_load_dword v7, v173, s[60:61] offset:2816 sc1
	global_load_dword v8, v173, s[60:61] offset:3072 sc1
	global_load_dword v9, v173, s[60:61] offset:3328 sc1
	global_load_dword v10, v173, s[60:61] offset:3584 sc1
	global_load_dword v11, v173, s[60:61] offset:3840 sc1
	global_load_dword v13, v173, s[2:3] sc1
	v_readlane_b32 s2, v250, 27
	v_readlane_b32 s3, v250, 28
	s_mov_b64 s[8:9], -1
	s_mov_b64 s[10:11], -1
	s_waitcnt vmcnt(11)
	v_add_u32_e32 v17, v0, v12
	s_nop 0
	global_load_dword v14, v173, s[2:3] sc1
	v_readlane_b32 s2, v250, 29
	v_readlane_b32 s3, v250, 30
	s_waitcnt vmcnt(11)
	v_add_u32_e32 v17, v17, v2
	s_waitcnt vmcnt(10)
	v_add_u32_e32 v17, v17, v3
	s_waitcnt vmcnt(9)
	v_add_u32_e32 v17, v17, v4
	s_waitcnt vmcnt(8)
	v_add_u32_e32 v17, v17, v5
	s_waitcnt vmcnt(7)
	v_add_u32_e32 v17, v17, v6
	global_load_dword v15, v173, s[2:3] sc1
	v_readlane_b32 s2, v250, 31
	v_readlane_b32 s3, v250, 32
	s_waitcnt vmcnt(7)
	v_add_u32_e32 v17, v17, v7
	s_waitcnt vmcnt(6)
	v_add_u32_e32 v17, v17, v8
	s_waitcnt vmcnt(5)
	v_add_u32_e32 v17, v17, v9
	s_waitcnt vmcnt(4)
	v_add_u32_e32 v17, v17, v10
	s_waitcnt vmcnt(3)
	v_add_u32_e32 v17, v17, v11
	global_load_dword v16, v173, s[2:3] sc1
	s_waitcnt vmcnt(3)
	v_add_u32_e32 v17, v17, v13
	s_waitcnt vmcnt(2)
	v_add_u32_e32 v17, v17, v14
	s_waitcnt vmcnt(1)
	v_add_u32_e32 v17, v17, v15
	s_waitcnt vmcnt(0)
	v_add_u32_e32 v17, v17, v16
	v_cmp_eq_u32_e32 vcc, s13, v17
	s_cbranch_vccnz .LBB0_588
	s_and_b32 s2, s14, 0xff
	s_cmp_eq_u32 s2, 0
	s_mov_b64 s[2:3], -1
	s_cbranch_scc1 .LBB0_593
	s_and_b64 vcc, exec, s[2:3]
	s_cbranch_vccz .LBB0_588

.LBB0_607:
	s_and_b32 s2, s22, 0xff
	s_mov_b64 s[18:19], -1
	s_cmp_lg_u32 s2, 0
	s_mov_b64 s[2:3], -1
	s_cbranch_scc0 .LBB0_610
	s_and_b64 vcc, exec, s[2:3]
	s_cbranch_vccz .LBB0_606

.LBB0_624:
	s_and_b32 s2, s20, 0xff
	s_mov_b64 s[16:17], -1
	s_cmp_lg_u32 s2, 0
	s_mov_b64 s[2:3], -1
	s_cbranch_scc0 .LBB0_627
	s_and_b64 vcc, exec, s[2:3]
	s_cbranch_vccz .LBB0_623

.LBB0_826:
	v_readlane_b32 s2, v250, 25
	v_readlane_b32 s3, v250, 26
	global_load_dword v12, v173, s[60:61] offset:1024 sc1
	global_load_dword v0, v173, s[60:61] offset:1280 sc1
	global_load_dword v2, v173, s[60:61] offset:1536 sc1
	global_load_dword v3, v173, s[60:61] offset:1792 sc1
	global_load_dword v4, v173, s[60:61] offset:2048 sc1
	global_load_dword v5, v173, s[60:61] offset:2304 sc1
	global_load_dword v6, v173, s[60:61] offset:2560 sc1
	global_load_dword v7, v173, s[60:61] offset:2816 sc1
	global_load_dword v8, v173, s[60:61] offset:3072 sc1
	global_load_dword v9, v173, s[60:61] offset:3328 sc1
	global_load_dword v10, v173, s[60:61] offset:3584 sc1
	global_load_dword v11, v173, s[60:61] offset:3840 sc1
	global_load_dword v13, v173, s[2:3] sc1
	v_readlane_b32 s2, v250, 27
	v_readlane_b32 s3, v250, 28
	s_mov_b64 s[4:5], -1
	s_mov_b64 s[10:11], -1
	s_waitcnt vmcnt(11)
	v_add_u32_e32 v17, v0, v12
	s_nop 0
	global_load_dword v14, v173, s[2:3] sc1
	v_readlane_b32 s2, v250, 29
	v_readlane_b32 s3, v250, 30
	s_waitcnt vmcnt(11)
	v_add_u32_e32 v17, v17, v2
	s_waitcnt vmcnt(10)
	v_add_u32_e32 v17, v17, v3
	s_waitcnt vmcnt(9)
	v_add_u32_e32 v17, v17, v4
	s_waitcnt vmcnt(8)
	v_add_u32_e32 v17, v17, v5
	s_waitcnt vmcnt(7)
	v_add_u32_e32 v17, v17, v6
	global_load_dword v15, v173, s[2:3] sc1
	v_readlane_b32 s2, v250, 31
	v_readlane_b32 s3, v250, 32
	s_waitcnt vmcnt(7)
	v_add_u32_e32 v17, v17, v7
	s_waitcnt vmcnt(6)
	v_add_u32_e32 v17, v17, v8
	s_waitcnt vmcnt(5)
	v_add_u32_e32 v17, v17, v9
	s_waitcnt vmcnt(4)
	v_add_u32_e32 v17, v17, v10
	s_waitcnt vmcnt(3)
	v_add_u32_e32 v17, v17, v11
	global_load_dword v16, v173, s[2:3] sc1
	s_waitcnt vmcnt(3)
	v_add_u32_e32 v17, v17, v13
	s_waitcnt vmcnt(2)
	v_add_u32_e32 v17, v17, v14
	s_waitcnt vmcnt(1)
	v_add_u32_e32 v17, v17, v15
	s_waitcnt vmcnt(0)
	v_add_u32_e32 v17, v17, v16
	v_cmp_eq_u32_e32 vcc, s13, v17
	s_cbranch_vccnz .LBB0_825
	s_and_b32 s2, s14, 0xff
	s_cmp_eq_u32 s2, 0
	s_mov_b64 s[2:3], -1
	s_cbranch_scc1 .LBB0_830
	s_and_b64 vcc, exec, s[2:3]
	s_cbranch_vccz .LBB0_825
